# baseline (speedup 1.0000x reference)
.LBB2_110:
	s_or_b64 exec, exec, s[0:1]
	v_bfe_u32 v65, v0, 6, 1
	v_bfe_u32 v1, v0, 3, 1
	v_lshl_or_b32 v46, v65, 1, v1
	v_lshrrev_b32_e32 v1, 3, v0
	v_and_b32_e32 v97, 15, v0
	v_and_b32_e32 v1, 48, v1
	v_or_b32_e32 v63, v1, v97
	v_mul_lo_u16_e32 v2, 20, v63
	v_lshrrev_b16_e32 v2, 7, v2
	v_and_b32_e32 v2, 14, v2
	v_or_b32_e32 v110, 64, v63
	v_add_u32_sdwa v6, v63, v2 dst_sel:DWORD dst_unused:UNUSED_PAD src0_sel:DWORD src1_sel:WORD_0
	v_mul_lo_u16_e32 v2, 0x4f, v110
	v_lshrrev_b16_e32 v2, 9, v2
	v_and_b32_e32 v2, 62, v2
	v_bfe_u32 v62, v0, 4, 2
	v_and_b32_e32 v47, 7, v0
	v_add_u32_e32 v10, v110, v2
	v_lshl_add_u32 v84, v62, 4, 0
	v_mad_u32_u24 v2, v46, 10, v47
	s_movk_i32 s0, 0x110
	v_lshrrev_b32_e32 v180, 4, v1
	v_lshrrev_b32_e32 v181, 1, v180
	v_and_b32_e32 v182, 1, v180
	v_lshl_or_b32 v181, v181, 5, v182
	v_add_u32_e32 v183, 4, v97
	v_add_u32_e32 v184, -8, v97
	v_cmp_gt_u32_e64 s[90:91], 4, v97
	v_cmp_lt_u32_e64 s[92:93], 11, v97
	v_mov_b32_e32 v188, 0xc0
	s_nop 0
	v_cndmask_b32_e64 v183, v183, v97, s[90:91]
	v_cndmask_b32_e64 v183, v183, v184, s[92:93]
	v_lshl_add_u32 v185, v183, 1, v181
	v_add_u32_e32 v186, 64, v185
	v_add_u32_e32 v187, 0x80, v185
	v_cmp_eq_u32_e32 vcc, 0xa4, v187
	s_nop 1
	v_cndmask_b32_e32 v187, v187, v188, vcc
	v_mul_u32_u24_e32 v189, 0x89, v185
	v_lshrrev_b32_e32 v189, 11, v189
	v_mad_i32_i24 v190, v189, -15, v185
	v_cmp_gt_u32_e32 vcc, 13, v190
	v_lshlrev_b32_e32 v191, 1, v189
	v_sub_u32_e32 v193, v185, v191
	v_mad_u32_u24 v98, v185, s0, v84
	v_cndmask_b32_e64 v196, 0, 1, vcc
	v_mul_u32_u24_e32 v189, 0x89, v186
	v_lshrrev_b32_e32 v189, 11, v189
	v_mad_i32_i24 v190, v189, -15, v186
	v_cmp_gt_u32_e32 vcc, 13, v190
	v_lshlrev_b32_e32 v191, 1, v189
	v_sub_u32_e32 v194, v186, v191
	v_mad_u32_u24 v111, v186, s0, v84
	v_cndmask_b32_e64 v197, 0, 1, vcc
	v_mul_u32_u24_e32 v189, 0x89, v187
	v_lshrrev_b32_e32 v189, 11, v189
	v_mad_i32_i24 v190, v189, -15, v187
	v_cmp_gt_u32_e32 vcc, 13, v190
	v_lshlrev_b32_e32 v191, 1, v189
	v_sub_u32_e32 v195, v187, v191
	v_mad_u32_u24 v117, v187, s0, v84
	v_cndmask_b32_e64 v198, 0, 1, vcc
	s_movk_i32 s0, 0x110
	s_waitcnt vmcnt(4)
	v_mad_u32_u24 v34, v2, s0, v84
	s_waitcnt lgkmcnt(0)
	s_barrier
	ds_read_b128 v[2:5], v34 offset:61200
	v_or_b32_e32 v64, 0x80, v63
	v_min_u32_e32 v22, 0xa8, v64
	v_mul_lo_u16_e32 v7, 0x4f, v22
	v_lshrrev_b16_e32 v23, 9, v7
	ds_read_b128 v[6:9], v98
	ds_read_b128 v[10:13], v111
	ds_read_b128 v[14:17], v34 offset:61264
	ds_read_b128 v[18:21], v98 offset:64
	v_and_b32_e32 v23, 30, v23
	s_waitcnt lgkmcnt(3)
	v_mfma_f32_16x16x32_f16 v[6:9], v[2:5], v[6:9], 0
	v_add_u32_e32 v26, v22, v23
	ds_read_b128 v[22:25], v111 offset:64
	ds_read_b128 v[26:29], v117
	ds_read_b128 v[30:33], v117 offset:64
	s_waitcnt lgkmcnt(3)
	v_mfma_f32_16x16x32_f16 v[6:9], v[14:17], v[18:21], v[6:9]
	ds_read_b128 v[18:21], v34 offset:61328
	v_add_u32_e32 v58, 1, v47
	v_add_u32_e32 v85, 2, v47
	v_mfma_f32_16x16x32_f16 v[10:13], v[2:5], v[10:13], 0
	v_lshl_or_b32 v86, s2, 9, v0
	v_ashrrev_i32_e32 v87, 31, v86
	v_lshlrev_b64 v[74:75], 4, v[86:87]
	s_waitcnt lgkmcnt(2)
	v_mfma_f32_16x16x32_f16 v[2:5], v[2:5], v[26:29], 0
	v_mad_u32_u24 v90, v46, 10, 20
	v_lshl_add_u64 v[70:71], s[60:61], 0, v[74:75]
	v_add_co_u32_e32 v42, vcc, 0x200000, v70
	v_mfma_f32_16x16x32_f16 v[10:13], v[14:17], v[22:25], v[10:13]
	s_nop 0
	v_addc_co_u32_e32 v43, vcc, 0, v71, vcc
	v_add_co_u32_e32 v50, vcc, 0x400000, v70
	s_waitcnt lgkmcnt(1)
	v_mfma_f32_16x16x32_f16 v[2:5], v[14:17], v[30:33], v[2:5]
	ds_read_b128 v[14:17], v98 offset:128
	ds_read_b128 v[22:25], v34 offset:61392
	ds_read_b128 v[26:29], v98 offset:192
	v_addc_co_u32_e32 v51, vcc, 0, v71, vcc
	s_waitcnt lgkmcnt(2)
	v_mfma_f32_16x16x32_f16 v[6:9], v[18:21], v[14:17], v[6:9]
	ds_read_b128 v[14:17], v111 offset:128
	ds_read_b128 v[30:33], v111 offset:192
	v_add_co_u32_e32 v52, vcc, 0x600000, v70
	s_waitcnt lgkmcnt(1)
	v_mfma_f32_16x16x32_f16 v[10:13], v[18:21], v[14:17], v[10:13]
	ds_read_b128 v[14:17], v117 offset:128
	ds_read_b128 v[34:37], v117 offset:192
	v_addc_co_u32_e32 v53, vcc, 0, v71, vcc
	s_waitcnt lgkmcnt(1)
	v_mfma_f32_16x16x32_f16 v[2:5], v[18:21], v[14:17], v[2:5]
	v_mad_u32_u24 v14, v46, 10, v58
	v_mad_u32_u24 v38, v14, s0, v84
	ds_read_b128 v[14:17], v38 offset:61200
	v_mfma_f32_16x16x32_f16 v[6:9], v[22:25], v[26:29], v[6:9]
	v_add_co_u32_e32 v54, vcc, 0x800000, v70
	s_mov_b32 s1, 0x200000
	v_mfma_f32_16x16x32_f16 v[10:13], v[22:25], v[30:33], v[10:13]
	v_addc_co_u32_e32 v55, vcc, 0, v71, vcc
	v_lshl_add_u64 v[82:83], s[62:63], 0, v[74:75]
	s_waitcnt lgkmcnt(1)
	v_mfma_f32_16x16x32_f16 v[2:5], v[22:25], v[34:37], v[2:5]
	ds_read_b128 v[18:21], v98 offset:272
	ds_read_b128 v[22:25], v38 offset:61264
	ds_read_b128 v[26:29], v98 offset:336
	s_mov_b32 s2, 0x400000
	s_mov_b32 s3, 0x600000
	s_waitcnt lgkmcnt(2)
	v_mfma_f32_16x16x32_f16 v[6:9], v[14:17], v[18:21], v[6:9]
	ds_read_b128 v[18:21], v111 offset:272
	ds_read_b128 v[30:33], v111 offset:336
	s_add_i32 s6, 0, 0x13890
	s_waitcnt lgkmcnt(1)
	v_mfma_f32_16x16x32_f16 v[10:13], v[14:17], v[18:21], v[10:13]
	ds_read_b128 v[18:21], v117 offset:272
	ds_read_b128 v[34:37], v117 offset:336
	s_waitcnt lgkmcnt(1)
	v_mfma_f32_16x16x32_f16 v[2:5], v[14:17], v[18:21], v[2:5]
	ds_read_b128 v[14:17], v38 offset:61328
	v_mfma_f32_16x16x32_f16 v[6:9], v[22:25], v[26:29], v[6:9]
	v_mfma_f32_16x16x32_f16 v[10:13], v[22:25], v[30:33], v[10:13]
	s_waitcnt lgkmcnt(1)
	v_mfma_f32_16x16x32_f16 v[2:5], v[22:25], v[34:37], v[2:5]
	ds_read_b128 v[18:21], v98 offset:400
	ds_read_b128 v[22:25], v38 offset:61392
	ds_read_b128 v[26:29], v98 offset:464
	s_waitcnt lgkmcnt(2)
	v_mfma_f32_16x16x32_f16 v[6:9], v[14:17], v[18:21], v[6:9]
	ds_read_b128 v[18:21], v111 offset:400
	ds_read_b128 v[30:33], v111 offset:464
	s_waitcnt lgkmcnt(1)
	v_mfma_f32_16x16x32_f16 v[10:13], v[14:17], v[18:21], v[10:13]
	ds_read_b128 v[18:21], v117 offset:400
	ds_read_b128 v[34:37], v117 offset:464
	s_waitcnt lgkmcnt(1)
	v_mfma_f32_16x16x32_f16 v[2:5], v[14:17], v[18:21], v[2:5]
	v_mad_u32_u24 v14, v46, 10, v85
	v_mad_u32_u24 v38, v14, s0, v84
	ds_read_b128 v[14:17], v38 offset:61200
	v_mfma_f32_16x16x32_f16 v[6:9], v[22:25], v[26:29], v[6:9]
	v_mfma_f32_16x16x32_f16 v[10:13], v[22:25], v[30:33], v[10:13]
	s_waitcnt lgkmcnt(1)
	v_mfma_f32_16x16x32_f16 v[2:5], v[22:25], v[34:37], v[2:5]
	ds_read_b128 v[18:21], v98 offset:544
	ds_read_b128 v[22:25], v38 offset:61264
	ds_read_b128 v[26:29], v98 offset:608
	s_waitcnt lgkmcnt(2)
	v_mfma_f32_16x16x32_f16 v[6:9], v[14:17], v[18:21], v[6:9]
	ds_read_b128 v[18:21], v111 offset:544
	ds_read_b128 v[30:33], v111 offset:608
	s_waitcnt lgkmcnt(1)
	v_mfma_f32_16x16x32_f16 v[10:13], v[14:17], v[18:21], v[10:13]
	ds_read_b128 v[18:21], v117 offset:544
	ds_read_b128 v[34:37], v117 offset:608
	s_waitcnt lgkmcnt(1)
	v_mfma_f32_16x16x32_f16 v[2:5], v[14:17], v[18:21], v[2:5]
	ds_read_b128 v[14:17], v38 offset:61328
	v_mfma_f32_16x16x32_f16 v[6:9], v[22:25], v[26:29], v[6:9]
	v_mfma_f32_16x16x32_f16 v[10:13], v[22:25], v[30:33], v[10:13]
	s_waitcnt lgkmcnt(1)
	v_mfma_f32_16x16x32_f16 v[2:5], v[22:25], v[34:37], v[2:5]
	ds_read_b128 v[18:21], v98 offset:672
	ds_read_b128 v[22:25], v38 offset:61392
	ds_read_b128 v[26:29], v98 offset:736
	v_mad_u32_u24 v38, v46, 10, 10
	s_waitcnt lgkmcnt(2)
	v_mfma_f32_16x16x32_f16 v[6:9], v[14:17], v[18:21], v[6:9]
	ds_read_b128 v[18:21], v111 offset:672
	ds_read_b128 v[30:33], v111 offset:736
	s_waitcnt lgkmcnt(1)
	v_mfma_f32_16x16x32_f16 v[10:13], v[14:17], v[18:21], v[10:13]
	ds_read_b128 v[18:21], v117 offset:672
	ds_read_b128 v[34:37], v117 offset:736
	s_waitcnt lgkmcnt(1)
	v_mfma_f32_16x16x32_f16 v[2:5], v[14:17], v[18:21], v[2:5]
	v_add_u32_e32 v14, v47, v38
	v_mad_u32_u24 v39, v14, s0, v84
	ds_read_b128 v[14:17], v39 offset:61200
	v_mfma_f32_16x16x32_f16 v[6:9], v[22:25], v[26:29], v[6:9]
	v_mfma_f32_16x16x32_f16 v[10:13], v[22:25], v[30:33], v[10:13]
	s_waitcnt lgkmcnt(1)
	v_mfma_f32_16x16x32_f16 v[2:5], v[22:25], v[34:37], v[2:5]
	ds_read_b128 v[18:21], v98 offset:4080
	ds_read_b128 v[22:25], v39 offset:61264
	ds_read_b128 v[26:29], v98 offset:4144
	s_waitcnt lgkmcnt(2)
	v_mfma_f32_16x16x32_f16 v[6:9], v[14:17], v[18:21], v[6:9]
	ds_read_b128 v[18:21], v111 offset:4080
	ds_read_b128 v[30:33], v111 offset:4144
	s_waitcnt lgkmcnt(1)
	v_mfma_f32_16x16x32_f16 v[10:13], v[14:17], v[18:21], v[10:13]
	ds_read_b128 v[18:21], v117 offset:4080
	ds_read_b128 v[34:37], v117 offset:4144
	s_waitcnt lgkmcnt(1)
	v_mfma_f32_16x16x32_f16 v[2:5], v[14:17], v[18:21], v[2:5]
	ds_read_b128 v[14:17], v39 offset:61328
	v_mfma_f32_16x16x32_f16 v[6:9], v[22:25], v[26:29], v[6:9]
	v_mfma_f32_16x16x32_f16 v[10:13], v[22:25], v[30:33], v[10:13]
	s_waitcnt lgkmcnt(1)
	v_mfma_f32_16x16x32_f16 v[2:5], v[22:25], v[34:37], v[2:5]
	ds_read_b128 v[18:21], v98 offset:4208
	ds_read_b128 v[22:25], v39 offset:61392
	ds_read_b128 v[26:29], v98 offset:4272
	s_waitcnt lgkmcnt(2)
	v_mfma_f32_16x16x32_f16 v[6:9], v[14:17], v[18:21], v[6:9]
	ds_read_b128 v[18:21], v111 offset:4208
	ds_read_b128 v[30:33], v111 offset:4272
	s_waitcnt lgkmcnt(1)
	v_mfma_f32_16x16x32_f16 v[10:13], v[14:17], v[18:21], v[10:13]
	ds_read_b128 v[18:21], v117 offset:4208
	ds_read_b128 v[34:37], v117 offset:4272
	s_waitcnt lgkmcnt(1)
	v_mfma_f32_16x16x32_f16 v[2:5], v[14:17], v[18:21], v[2:5]
	v_add_u32_e32 v14, v58, v38
	v_mad_u32_u24 v39, v14, s0, v84
	ds_read_b128 v[14:17], v39 offset:61200
	v_mfma_f32_16x16x32_f16 v[6:9], v[22:25], v[26:29], v[6:9]
	v_mfma_f32_16x16x32_f16 v[10:13], v[22:25], v[30:33], v[10:13]
	s_waitcnt lgkmcnt(1)
	v_mfma_f32_16x16x32_f16 v[2:5], v[22:25], v[34:37], v[2:5]
	ds_read_b128 v[18:21], v98 offset:4352
	ds_read_b128 v[22:25], v39 offset:61264
	ds_read_b128 v[26:29], v98 offset:4416
	s_waitcnt lgkmcnt(2)
	v_mfma_f32_16x16x32_f16 v[6:9], v[14:17], v[18:21], v[6:9]
	ds_read_b128 v[18:21], v111 offset:4352
	ds_read_b128 v[30:33], v111 offset:4416
	s_waitcnt lgkmcnt(1)
	v_mfma_f32_16x16x32_f16 v[10:13], v[14:17], v[18:21], v[10:13]
	ds_read_b128 v[18:21], v117 offset:4352
	ds_read_b128 v[34:37], v117 offset:4416
	s_waitcnt lgkmcnt(1)
	v_mfma_f32_16x16x32_f16 v[2:5], v[14:17], v[18:21], v[2:5]
	ds_read_b128 v[14:17], v39 offset:61328
	v_mfma_f32_16x16x32_f16 v[6:9], v[22:25], v[26:29], v[6:9]
	v_mfma_f32_16x16x32_f16 v[10:13], v[22:25], v[30:33], v[10:13]
	s_waitcnt lgkmcnt(1)
	v_mfma_f32_16x16x32_f16 v[2:5], v[22:25], v[34:37], v[2:5]
	ds_read_b128 v[18:21], v98 offset:4480
	ds_read_b128 v[22:25], v39 offset:61392
	ds_read_b128 v[26:29], v98 offset:4544
	s_waitcnt lgkmcnt(2)
	v_mfma_f32_16x16x32_f16 v[6:9], v[14:17], v[18:21], v[6:9]
	ds_read_b128 v[18:21], v111 offset:4480
	ds_read_b128 v[30:33], v111 offset:4544
	s_waitcnt lgkmcnt(1)
	v_mfma_f32_16x16x32_f16 v[10:13], v[14:17], v[18:21], v[10:13]
	ds_read_b128 v[18:21], v117 offset:4480
	ds_read_b128 v[34:37], v117 offset:4544
	s_waitcnt lgkmcnt(1)
	v_mfma_f32_16x16x32_f16 v[2:5], v[14:17], v[18:21], v[2:5]
	v_add_u32_e32 v14, v85, v38
	v_mad_u32_u24 v38, v14, s0, v84
	ds_read_b128 v[14:17], v38 offset:61200
	v_mfma_f32_16x16x32_f16 v[6:9], v[22:25], v[26:29], v[6:9]
	v_mfma_f32_16x16x32_f16 v[10:13], v[22:25], v[30:33], v[10:13]
	s_waitcnt lgkmcnt(1)
	v_mfma_f32_16x16x32_f16 v[2:5], v[22:25], v[34:37], v[2:5]
	ds_read_b128 v[18:21], v98 offset:4624
	ds_read_b128 v[22:25], v38 offset:61264
	ds_read_b128 v[26:29], v98 offset:4688
	s_waitcnt lgkmcnt(2)
	v_mfma_f32_16x16x32_f16 v[6:9], v[14:17], v[18:21], v[6:9]
	ds_read_b128 v[18:21], v111 offset:4624
	ds_read_b128 v[30:33], v111 offset:4688
	s_waitcnt lgkmcnt(1)
	v_mfma_f32_16x16x32_f16 v[10:13], v[14:17], v[18:21], v[10:13]
	ds_read_b128 v[18:21], v117 offset:4624
	ds_read_b128 v[34:37], v117 offset:4688
	s_waitcnt lgkmcnt(1)
	v_mfma_f32_16x16x32_f16 v[2:5], v[14:17], v[18:21], v[2:5]
	ds_read_b128 v[14:17], v38 offset:61328
	ds_read_b128 v[18:21], v98 offset:4752
	v_mfma_f32_16x16x32_f16 v[6:9], v[22:25], v[26:29], v[6:9]
	v_mfma_f32_16x16x32_f16 v[10:13], v[22:25], v[30:33], v[10:13]
	s_waitcnt lgkmcnt(2)
	v_mfma_f32_16x16x32_f16 v[22:25], v[22:25], v[34:37], v[2:5]
	s_nop 2
	ds_read_b128 v[2:5], v111 offset:4752
	ds_read_b128 v[26:29], v38 offset:61392
	ds_read_b128 v[30:33], v98 offset:4816
	ds_read_b128 v[34:37], v117 offset:4752
	ds_read_b128 v[38:41], v111 offset:4816
	s_waitcnt lgkmcnt(5)
	v_mfma_f32_16x16x32_f16 v[18:21], v[14:17], v[18:21], v[6:9]
	s_waitcnt lgkmcnt(4)
	v_mfma_f32_16x16x32_f16 v[10:13], v[14:17], v[2:5], v[10:13]
	s_nop 0
	global_load_dwordx4 v[6:9], v[70:71], off nt
	global_load_dwordx4 v[2:5], v[42:43], off nt
	ds_read_b128 v[42:45], v117 offset:4816
	s_waitcnt lgkmcnt(2)
	v_mfma_f32_16x16x32_f16 v[14:17], v[14:17], v[34:37], v[22:25]
	s_nop 2
	v_add_u32_e32 v22, v47, v90
	v_mad_u32_u24 v56, v22, s0, v84
	ds_read_b128 v[22:25], v56 offset:61200
	v_mfma_f32_16x16x32_f16 v[18:21], v[26:29], v[30:33], v[18:21]
	ds_read_b128 v[30:33], v98 offset:8160
	s_waitcnt lgkmcnt(3)
	v_mfma_f32_16x16x32_f16 v[10:13], v[26:29], v[38:41], v[10:13]
	s_waitcnt lgkmcnt(2)
	v_mfma_f32_16x16x32_f16 v[14:17], v[26:29], v[42:45], v[14:17]
	ds_read_b128 v[26:29], v111 offset:8160
	ds_read_b128 v[34:37], v56 offset:61264
	ds_read_b128 v[38:41], v98 offset:8224
	s_waitcnt lgkmcnt(3)
	v_mfma_f32_16x16x32_f16 v[18:21], v[22:25], v[30:33], v[18:21]
	ds_read_b128 v[30:33], v117 offset:8160
	ds_read_b128 v[42:45], v111 offset:8224
	ds_read_b128 v[46:49], v117 offset:8224
	s_waitcnt lgkmcnt(5)
	v_mfma_f32_16x16x32_f16 v[26:29], v[22:25], v[26:29], v[10:13]
	s_waitcnt lgkmcnt(2)
	v_mfma_f32_16x16x32_f16 v[22:25], v[22:25], v[30:33], v[14:17]
	s_nop 2
	global_load_dwordx4 v[14:17], v[50:51], off nt
	global_load_dwordx4 v[10:13], v[52:53], off nt
	ds_read_b128 v[30:33], v56 offset:61328
	v_mfma_f32_16x16x32_f16 v[18:21], v[34:37], v[38:41], v[18:21]
	ds_read_b128 v[38:41], v98 offset:8288
	s_waitcnt lgkmcnt(3)
	v_mfma_f32_16x16x32_f16 v[26:29], v[34:37], v[42:45], v[26:29]
	s_waitcnt lgkmcnt(2)
	v_mfma_f32_16x16x32_f16 v[22:25], v[34:37], v[46:49], v[22:25]
	ds_read_b128 v[34:37], v111 offset:8288
	ds_read_b128 v[42:45], v56 offset:61392
	ds_read_b128 v[46:49], v98 offset:8352
	v_add_co_u32_e32 v56, vcc, 0xa00000, v70
	s_waitcnt lgkmcnt(3)
	v_mfma_f32_16x16x32_f16 v[38:41], v[30:33], v[38:41], v[18:21]
	s_nop 2
	ds_read_b128 v[18:21], v117 offset:8288
	ds_read_b128 v[50:53], v111 offset:8352
	v_addc_co_u32_e32 v57, vcc, 0, v71, vcc
	s_waitcnt lgkmcnt(2)
	v_mfma_f32_16x16x32_f16 v[38:41], v[42:45], v[46:49], v[38:41]
	v_add_u32_e32 v46, v58, v90
	v_mad_u32_u24 v80, v46, s0, v84
	v_add_co_u32_e32 v76, vcc, 0xc00000, v70
	v_mfma_f32_16x16x32_f16 v[26:29], v[30:33], v[34:37], v[26:29]
	ds_read_b128 v[34:37], v117 offset:8352
	v_addc_co_u32_e32 v77, vcc, 0, v71, vcc
	s_waitcnt lgkmcnt(2)
	v_mfma_f32_16x16x32_f16 v[30:33], v[30:33], v[18:21], v[22:25]
	s_nop 2
	global_load_dwordx4 v[22:25], v[54:55], off nt
	global_load_dwordx4 v[18:21], v[56:57], off nt
	ds_read_b128 v[46:49], v80 offset:61200
	v_add_co_u32_e32 v78, vcc, 0xe00000, v70
	s_waitcnt lgkmcnt(2)
	v_mfma_f32_16x16x32_f16 v[26:29], v[42:45], v[50:53], v[26:29]
	ds_read_b128 v[50:53], v98 offset:8432
	v_addc_co_u32_e32 v79, vcc, 0, v71, vcc
	s_waitcnt lgkmcnt(2)
	v_mfma_f32_16x16x32_f16 v[30:33], v[42:45], v[34:37], v[30:33]
	ds_read_b128 v[34:37], v111 offset:8432
	ds_read_b128 v[42:45], v80 offset:61264
	ds_read_b128 v[54:57], v98 offset:8496
	v_add_co_u32_e32 v74, vcc, s1, v82
	s_waitcnt lgkmcnt(3)
	v_mfma_f32_16x16x32_f16 v[38:41], v[46:49], v[50:53], v[38:41]
	ds_read_b128 v[50:53], v117 offset:8432
	ds_read_b128 v[58:61], v111 offset:8496
	ds_read_b128 v[70:73], v117 offset:8496
	v_addc_co_u32_e32 v75, vcc, 0, v83, vcc
	s_waitcnt lgkmcnt(5)
	v_mfma_f32_16x16x32_f16 v[66:69], v[46:49], v[34:37], v[26:29]
	global_load_dwordx4 v[34:37], v[76:77], off nt
	s_nop 1
	global_load_dwordx4 v[26:29], v[78:79], off nt
	v_add_co_u32_e32 v88, vcc, s2, v82
	s_waitcnt lgkmcnt(2)
	v_mfma_f32_16x16x32_f16 v[30:33], v[46:49], v[50:53], v[30:33]
	ds_read_b128 v[46:49], v80 offset:61328
	v_addc_co_u32_e32 v89, vcc, 0, v83, vcc
	v_mfma_f32_16x16x32_f16 v[38:41], v[42:45], v[54:57], v[38:41]
	ds_read_b128 v[54:57], v98 offset:8560
	s_movk_i32 s2, 0xa9
	s_waitcnt lgkmcnt(3)
	v_mfma_f32_16x16x32_f16 v[50:53], v[42:45], v[58:61], v[66:69]
	s_waitcnt lgkmcnt(2)
	v_mfma_f32_16x16x32_f16 v[42:45], v[42:45], v[70:73], v[30:33]
	ds_read_b128 v[58:61], v111 offset:8560
	ds_read_b128 v[66:69], v80 offset:61392
	ds_read_b128 v[70:73], v98 offset:8624
	s_waitcnt lgkmcnt(3)
	v_mfma_f32_16x16x32_f16 v[54:57], v[46:49], v[54:57], v[38:41]
	s_nop 2
	ds_read_b128 v[74:77], v117 offset:8560
	ds_read_b128 v[78:81], v111 offset:8624
	s_waitcnt lgkmcnt(4)
	v_mfma_f32_16x16x32_f16 v[50:53], v[46:49], v[58:61], v[50:53]
	ds_read_b128 v[58:61], v117 offset:8624
	s_waitcnt lgkmcnt(2)
	v_mfma_f32_16x16x32_f16 v[42:45], v[46:49], v[74:77], v[42:45]
	v_mfma_f32_16x16x32_f16 v[46:49], v[66:69], v[70:73], v[54:57]
	ds_read_b128 v[70:73], v98 offset:8704
	s_nop 1
	v_add_u32_e32 v54, v85, v90
	v_mad_u32_u24 v92, v54, s0, v84
	ds_read_b128 v[54:57], v92 offset:61200
	s_waitcnt lgkmcnt(3)
	v_mfma_f32_16x16x32_f16 v[50:53], v[66:69], v[78:81], v[50:53]
	v_add_co_u32_e32 v90, vcc, s3, v82
	s_add_i32 s0, 0, 0x13550
	s_waitcnt lgkmcnt(2)
	v_mfma_f32_16x16x32_f16 v[58:61], v[66:69], v[58:61], v[42:45]
	s_nop 2
	ds_read_b128 v[42:45], v111 offset:8704
	ds_read_b128 v[66:69], v92 offset:61264
	ds_read_b128 v[74:77], v98 offset:8768
	v_addc_co_u32_e32 v91, vcc, 0, v83, vcc
	s_waitcnt lgkmcnt(3)
	v_mfma_f32_16x16x32_f16 v[70:73], v[54:57], v[70:73], v[46:49]
	ds_read_b128 v[78:81], v117 offset:8704
	ds_read_b128 v[82:85], v111 offset:8768
	v_cmp_gt_u32_e64 s[2:3], s2, v64
	v_cmp_eq_u32_e32 vcc, 0, v97
	s_waitcnt lgkmcnt(4)
	v_mfma_f32_16x16x32_f16 v[50:53], v[54:57], v[42:45], v[50:53]
	ds_read_b128 v[88:91], v117 offset:8768
	s_waitcnt lgkmcnt(2)
	v_mfma_f32_16x16x32_f16 v[54:57], v[54:57], v[78:81], v[58:61]
	s_nop 2
	ds_read_b128 v[58:61], v92 offset:61328
	ds_read_b128 v[92:95], v92 offset:61392
	ds_read_b128 v[78:81], v98 offset:8832
	ds_read_b128 v[98:101], v98 offset:8896
	ds_read_b128 v[106:109], v111 offset:8832
	ds_read_b128 v[118:121], v111 offset:8896
	ds_read_b128 v[122:125], v117 offset:8832
	ds_read_b128 v[126:129], v117 offset:8896
	v_mfma_f32_16x16x32_f16 v[102:105], v[66:69], v[74:77], v[70:73]
	s_waitcnt lgkmcnt(9)
	v_mfma_f32_16x16x32_f16 v[50:53], v[66:69], v[82:85], v[50:53]
	s_nop 0
	v_lshlrev_b32_e32 v70, 2, v62
	v_lshl_or_b32 v73, v65, 4, v70
	v_lshl_add_u32 v75, v73, 2, 0
	s_waitcnt lgkmcnt(8)
	v_mfma_f32_16x16x32_f16 v[66:69], v[66:69], v[88:91], v[54:57]
	v_add_u32_e32 v65, 0x13810, v75
	v_min_u32_e32 v72, 0xaf, v64
	v_lshl_add_u32 v70, v63, 2, s0
	s_waitcnt lgkmcnt(5)
	v_mfma_f32_16x16x32_f16 v[54:57], v[58:61], v[78:81], v[102:105]
	v_lshl_add_u32 v71, v110, 2, s0
	v_lshl_add_u32 v72, v72, 2, s0
	ds_read_b32 v65, v65
	ds_read_b32 v79, v70
	ds_read_b32 v78, v71
	ds_read_b32 v77, v72
	s_waitcnt lgkmcnt(7)
	v_mfma_f32_16x16x32_f16 v[80:83], v[58:61], v[106:109], v[50:53]
	s_movk_i32 s0, 0x69
	v_cmp_gt_u32_e64 s[0:1], s0, v63
	s_waitcnt lgkmcnt(5)
	v_mfma_f32_16x16x32_f16 v[58:61], v[58:61], v[122:125], v[66:69]
	v_mfma_f32_16x16x32_f16 v[50:53], v[92:95], v[98:101], v[54:57]
	v_mfma_f32_16x16x32_f16 v[54:57], v[92:95], v[118:121], v[80:83]
	s_waitcnt lgkmcnt(4)
	v_mfma_f32_16x16x32_f16 v[58:61], v[92:95], v[126:129], v[58:61]
	s_waitcnt lgkmcnt(2)
	s_nop 3
	v_or_b32_e32 v69, 1, v73
	v_or_b32_e32 v64, 2, v73
	v_or_b32_e32 v152, 3, v73
	v_lshl_add_u32 v71, v69, 2, 0
	v_lshl_add_u32 v66, v64, 2, 0
	v_lshl_add_u32 v153, v152, 2, 0
	v_add_u32_e32 v160, 0x13810, v71
	v_add_u32_e32 v161, 0x13810, v66
	v_add_u32_e32 v162, 0x13810, v153
	v_mov_b32_e32 v156, 0x13550
	v_lshl_add_u32 v157, v193, 2, v156
	v_lshl_add_u32 v158, v194, 2, v156
	v_lshl_add_u32 v159, v195, 2, v156
	ds_read_b32 v79, v157
	ds_read_b32 v78, v158
	ds_read_b32 v77, v159
	ds_read_b32 v160, v160
	ds_read_b32 v161, v161
	ds_read_b32 v162, v162
	v_mov_b32_e32 v155, 0xff800000
	s_waitcnt lgkmcnt(3)
	v_mul_f32_e32 v164, v50, v79
	v_mul_f32_e32 v165, v54, v78
	v_mul_f32_e32 v166, v58, v77
	v_mul_f32_e32 v164, v65, v164
	v_mul_f32_e32 v165, v65, v165
	v_mul_f32_e32 v166, v65, v166
	v_mul_f32_e32 v167, v51, v79
	v_mul_f32_e32 v168, v55, v78
	v_mul_f32_e32 v169, v59, v77
	v_mul_f32_e32 v170, v52, v79
	v_mul_f32_e32 v171, v56, v78
	v_mul_f32_e32 v172, v60, v77
	v_mul_f32_e32 v173, v53, v79
	v_mul_f32_e32 v174, v57, v78
	v_mul_f32_e32 v175, v61, v77
	s_waitcnt lgkmcnt(0)
	v_mul_f32_e32 v167, v160, v167
	v_mul_f32_e32 v168, v160, v168
	v_mul_f32_e32 v169, v160, v169
	v_mul_f32_e32 v170, v161, v170
	v_mul_f32_e32 v171, v161, v171
	v_mul_f32_e32 v172, v161, v172
	v_mul_f32_e32 v173, v162, v173
	v_mul_f32_e32 v174, v162, v174
	v_mul_f32_e32 v175, v162, v175
	v_cmp_ne_u32_e64 s[8:9], 0, v196
	v_cmp_ne_u32_e64 s[0:1], 0, v197
	v_cmp_ne_u32_e64 s[2:3], 0, v198
	v_cndmask_b32_e64 v164, v155, v164, s[8:9]
	v_cndmask_b32_e64 v167, v155, v167, s[8:9]
	v_cndmask_b32_e64 v170, v155, v170, s[8:9]
	v_cndmask_b32_e64 v173, v155, v173, s[8:9]
	v_cndmask_b32_e64 v165, v155, v165, s[0:1]
	v_cndmask_b32_e64 v166, v155, v166, s[2:3]
	v_cndmask_b32_e64 v168, v155, v168, s[0:1]
	v_cndmask_b32_e64 v169, v155, v169, s[2:3]
	v_cndmask_b32_e64 v171, v155, v171, s[0:1]
	v_cndmask_b32_e64 v172, v155, v172, s[2:3]
	v_cndmask_b32_e64 v174, v155, v174, s[0:1]
	v_cndmask_b32_e64 v175, v155, v175, s[2:3]
	v_max_f32_e32 v176, 0xff800000, v164
	v_max_f32_e32 v177, 0xff800000, v167
	v_max_f32_e32 v178, 0xff800000, v170
	v_max_f32_e32 v179, 0xff800000, v173
	v_max3_f32 v176, v176, v165, v166
	v_max3_f32 v177, v177, v168, v169
	v_max3_f32 v178, v178, v171, v172
	v_max3_f32 v179, v179, v174, v175
	v_max_f32_dpp v176, v176, v176 quad_perm:[1,0,3,2] row_mask:0xf bank_mask:0xf
	v_max_f32_dpp v177, v177, v177 quad_perm:[1,0,3,2] row_mask:0xf bank_mask:0xf
	v_max_f32_dpp v178, v178, v178 quad_perm:[1,0,3,2] row_mask:0xf bank_mask:0xf
	v_max_f32_dpp v179, v179, v179 quad_perm:[1,0,3,2] row_mask:0xf bank_mask:0xf
	v_max_f32_dpp v176, v176, v176 quad_perm:[2,3,0,1] row_mask:0xf bank_mask:0xf
	v_max_f32_dpp v177, v177, v177 quad_perm:[2,3,0,1] row_mask:0xf bank_mask:0xf
	v_max_f32_dpp v178, v178, v178 quad_perm:[2,3,0,1] row_mask:0xf bank_mask:0xf
	v_max_f32_dpp v179, v179, v179 quad_perm:[2,3,0,1] row_mask:0xf bank_mask:0xf
	v_max_f32_dpp v176, v176, v176 row_half_mirror row_mask:0xf bank_mask:0xf
	v_max_f32_dpp v177, v177, v177 row_half_mirror row_mask:0xf bank_mask:0xf
	v_max_f32_dpp v178, v178, v178 row_half_mirror row_mask:0xf bank_mask:0xf
	v_max_f32_dpp v179, v179, v179 row_half_mirror row_mask:0xf bank_mask:0xf
	v_max_f32_dpp v176, v176, v176 row_mirror row_mask:0xf bank_mask:0xf
	v_max_f32_dpp v177, v177, v177 row_mirror row_mask:0xf bank_mask:0xf
	v_max_f32_dpp v178, v178, v178 row_mirror row_mask:0xf bank_mask:0xf
	v_max_f32_dpp v179, v179, v179 row_mirror row_mask:0xf bank_mask:0xf
	v_and_b32_e32 v58, 0x180, v0
	v_add_u32_e32 v58, s6, v58
	v_lshl_add_u32 v58, v73, 2, v58
	s_and_saveexec_b64 s[6:7], vcc
	ds_write_b128 v58, v[176:179]
	s_or_b64 exec, exec, s[6:7]
	v_mov_b32_e32 v76, v164
	v_mov_b32_e32 v74, v165
	v_mov_b32_e32 v72, v166
	v_mov_b32_e32 v70, v167
	v_mov_b32_e32 v68, v168
	v_mov_b32_e32 v67, v169
	v_mov_b32_e32 v65, v170
	v_mov_b32_e32 v59, v171
	v_mov_b32_e32 v56, v172
	v_mov_b32_e32 v53, v173
	v_mov_b32_e32 v52, v174
	v_mov_b32_e32 v50, v175
	v_mov_b32_e32 v54, v152
	v_mov_b32_e32 v55, v153
	v_add_u32_e32 v51, 0x13890, v75
	s_waitcnt lgkmcnt(0)
	s_barrier
	v_add_u32_e32 v152, 0x13890, v75
	ds_read_b128 v[156:159], v152
	ds_read_b128 v[160:163], v152 offset:128
	ds_read_b128 v[164:167], v152 offset:256
	ds_read_b128 v[168:171], v152 offset:384
	v_lshlrev_b32_e32 v51, 3, v62
	v_lshlrev_b32_e32 v60, 8, v73
	v_or_b32_e32 v172, v63, v60
	s_waitcnt lgkmcnt(0)
	v_max_f32_e32 v173, v156, v160
	v_max_f32_e32 v174, v157, v161
	v_max_f32_e32 v175, v158, v162
	v_max_f32_e32 v176, v159, v163
	v_max3_f32 v173, v173, v164, v168
	v_max3_f32 v174, v174, v165, v169
	v_max3_f32 v175, v175, v166, v170
	v_max3_f32 v176, v176, v167, v171
	v_add_f32_e32 v173, 0xbb102de0, v173
	v_add_f32_e32 v174, 0xbb102de0, v174
	v_add_f32_e32 v175, 0xbb102de0, v175
	v_add_f32_e32 v176, 0xbb102de0, v176
	v_cmp_ge_f32_e64 s[90:91], v76, v173
	v_cmp_ge_f32_e64 s[92:93], v74, v173
	v_cmp_ge_f32_e64 s[94:95], v72, v173
	v_cmp_ge_f32_e64 s[96:97], v70, v174
	v_cmp_ge_f32_e64 s[98:99], v68, v174
	v_cmp_ge_f32_e64 s[60:61], v67, v174
	v_cmp_ge_f32_e64 s[62:63], v65, v175
	v_cmp_ge_f32_e64 s[88:89], v59, v175
	v_cmp_ge_f32_e64 s[6:7], v56, v175
	v_cmp_ge_f32_e64 s[8:9], v53, v176
	v_cmp_ge_f32_e64 s[2:3], v52, v176
	v_cmp_ge_f32_e64 s[80:81], v50, v176
	s_bcnt1_i32_b64 s13, s[90:91]
	s_bcnt1_i32_b64 s1, s[92:93]
	s_add_u32 s13, s13, s1
	s_bcnt1_i32_b64 s1, s[94:95]
	s_add_u32 s13, s13, s1
	s_bcnt1_i32_b64 s1, s[96:97]
	s_add_u32 s13, s13, s1
	s_bcnt1_i32_b64 s1, s[98:99]
	s_add_u32 s13, s13, s1
	s_bcnt1_i32_b64 s1, s[60:61]
	s_add_u32 s13, s13, s1
	s_bcnt1_i32_b64 s1, s[62:63]
	s_add_u32 s13, s13, s1
	s_bcnt1_i32_b64 s1, s[88:89]
	s_add_u32 s13, s13, s1
	s_bcnt1_i32_b64 s1, s[6:7]
	s_add_u32 s13, s13, s1
	s_bcnt1_i32_b64 s1, s[8:9]
	s_add_u32 s13, s13, s1
	s_bcnt1_i32_b64 s1, s[2:3]
	s_add_u32 s13, s13, s1
	s_bcnt1_i32_b64 s1, s[80:81]
	s_add_u32 s13, s13, s1
	s_cmp_eq_u32 s13, 0
	s_cbranch_scc1 .Lmy_list_done
	v_mov_b32_e32 v177, 0x13d90
	v_mov_b32_e32 v178, s13
	s_mov_b64 exec, 1
	ds_add_rtn_u32 v179, v177, v178
	s_mov_b64 exec, -1
	s_waitcnt lgkmcnt(0)
	v_readfirstlane_b32 s0, v179
	s_and_saveexec_b64 s[82:83], s[90:91]
	s_cbranch_execz .Lmy_list_skip0
	v_mbcnt_lo_u32_b32 v180, s90, 0
	v_mbcnt_hi_u32_b32 v180, s91, v180
	v_add_u32_e32 v181, 0x0, v60
	v_or_b32_e32 v181, v181, v193
	v_add_lshl_u32 v180, v180, s0, 1
	ds_write_b16 v180, v181
	s_bcnt1_i32_b64 s1, s[90:91]
	s_add_u32 s0, s0, s1
